# alternating per-tile s_setprio + barrier placed 3 fragments early
# speedup vs baseline: 1.0108x; 1.0108x over previous
.LBB0_733:
	s_or_b64 exec, exec, s[8:9]
	s_movk_i32 s4, 0xf0
	s_cmp_lg_u32 0, -1
	v_lshlrev_b32_e32 v39, 8, v141
	v_bitop3_b32 v80, v142, s4, v136 bitop3:0x48
	s_cselect_b32 s10, 0, 0
	v_cvt_pk_bf16_f32 v96, v134, v135
	v_cvt_pk_bf16_f32 v97, v132, v133
	v_cvt_pk_bf16_f32 v98, v130, v131
	v_cvt_pk_bf16_f32 v99, v128, v129
	v_cvt_pk_bf16_f32 v100, v126, v127
	v_cvt_pk_bf16_f32 v101, v124, v125
	v_cvt_pk_bf16_f32 v102, v122, v123
	v_cvt_pk_bf16_f32 v103, v120, v121
	v_cvt_pk_bf16_f32 v104, v70, v71
	v_cvt_pk_bf16_f32 v105, v74, v75
	v_cvt_pk_bf16_f32 v106, v64, v65
	v_cvt_pk_bf16_f32 v107, v68, v69
	v_cvt_pk_bf16_f32 v108, v60, v61
	v_cvt_pk_bf16_f32 v109, v66, v67
	v_cvt_pk_bf16_f32 v110, v56, v57
	v_cvt_pk_bf16_f32 v111, v58, v59
	v_cvt_pk_bf16_f32 v112, v112, v113
	v_cvt_pk_bf16_f32 v113, v118, v119
	v_cvt_pk_bf16_f32 v114, v114, v115
	v_cvt_pk_bf16_f32 v115, v116, v117
	v_cvt_pk_bf16_f32 v116, v78, v79
	v_cvt_pk_bf16_f32 v117, v76, v77
	v_cvt_pk_bf16_f32 v118, v72, v73
	v_cvt_pk_bf16_f32 v119, v62, v63
	v_cvt_pk_bf16_f32 v120, v52, v53
	v_cvt_pk_bf16_f32 v121, v54, v55
	v_cvt_pk_bf16_f32 v122, v46, v47
	v_cvt_pk_bf16_f32 v123, v50, v51
	v_cvt_pk_bf16_f32 v124, v44, v45
	v_cvt_pk_bf16_f32 v125, v48, v49
	v_cvt_pk_bf16_f32 v126, v40, v41
	v_cvt_pk_bf16_f32 v127, v42, v43
	v_readlane_b32 s100, v250, 8
	v_mbcnt_lo_u32_b32 v68, -1, 0
	v_mbcnt_hi_u32_b32 v68, -1, v68
	s_nop 1
	v_add_u32_e32 v69, s100, v68
	v_lshrrev_b32_e32 v70, 3, v69
	v_and_b32_e32 v71, 7, v69
	v_lshrrev_b32_e32 v72, 2, v71
	v_bfe_u32 v73, v71, 1, 1
	v_and_b32_e32 v74, 1, v71
	v_lshlrev_b32_e32 v74, 1, v74
	v_lshl_add_u32 v75, v72, 2, v74
	v_bfe_u32 v76, v70, 1, 3
	v_xor_b32_e32 v77, v75, v76
	v_add_u32_e32 v78, 1, v75
	v_xor_b32_e32 v78, v78, v76
	v_lshlrev_b32_e32 v79, 7, v70
	v_lshl_add_u32 v79, v73, 3, v79
	v_lshl_add_u32 v64, v77, 4, v79
	v_lshl_add_u32 v65, v78, 4, v79
	v_add_u32_e32 v66, 0x2000, v64
	v_add_u32_e32 v67, 0x2000, v65
	v_or_b32_e32 v81, v39, v80
	s_add_i32 s15, s10, 0x10000
	v_and_b32_e32 v82, 6, v137
	v_lshrrev_b32_e32 v84, 4, v136
	s_waitcnt vmcnt(0)
	s_waitcnt vmcnt(0)
	s_add_i32 s11, s10, 0x12000
	v_lshl_add_u32 v83, v139, 7, s10
	v_bitop3_b32 v85, v84, v82, 7 bitop3:0x6c
	v_and_b32_e32 v86, 8, v138
	v_or_b32_e32 v82, 1, v82
	v_add_u32_e32 v225, s15, v81
	s_waitcnt vmcnt(4)
	ds_write_b128 v225, v[24:27] offset:0
	v_lshlrev_b32_e32 v85, 4, v85
	v_add_u32_e32 v87, v83, v86
	v_bitop3_b32 v82, v84, v82, 7 bitop3:0x6c
	v_add3_u32 v226, v80, s11, v39
	ds_write_b128 v226, v[28:31] offset:0
	v_lshlrev_b32_e32 v82, 4, v82
	v_add_u32_e32 v227, v87, v85
	ds_write_b64 v64, v[12:13] offset:0
	v_lshrrev_b32_e32 v32, 5, v136
	v_add_u32_e32 v83, 0x2000, v83
	v_or_b32_e32 v84, v85, v86
	v_add_u32_e32 v228, v87, v82
	ds_write_b64 v65, v[14:15] offset:0
	v_xor_b32_e32 v32, v32, v137
	v_or_b32_e32 v86, v82, v86
	v_add_u32_e32 v229, v84, v83
	ds_write_b64 v66, v[4:5] offset:0
	v_lshlrev_b32_e32 v32, 4, v32
	v_add_u32_e32 v184, v86, v83
	ds_write_b64 v67, v[6:7] offset:0
	v_lshlrev_b32_e32 v33, 8, v143
	v_and_b32_e32 v32, 16, v32
	v_bfe_u32 v35, v137, 1, 3
	s_waitcnt vmcnt(4)
	ds_write_b128 v225, v[20:23] offset:0x4000
	v_lshlrev_b32_e32 v36, 5, v35
	v_add3_u32 v32, v33, s15, v32
	s_movk_i32 s16, 0x60
	ds_write_b128 v226, v[16:19] offset:0x4000
	v_xad_u32 v204, v36, s16, v32
	s_movk_i32 s16, 0x80
	ds_write_b64 v64, v[8:9] offset:0x4000
	v_xad_u32 v205, v36, s16, v32
	s_movk_i32 s16, 0xa0
	ds_write_b64 v65, v[10:11] offset:0x4000
	s_add_u32 s8, s6, 0x100
	v_xad_u32 v206, v36, s16, v32
	s_movk_i32 s16, 0xc0
	ds_write_b64 v66, v[0:1] offset:0x4000
	s_addc_u32 s9, s7, 0
	v_xad_u32 v207, v36, s16, v32
	s_movk_i32 s16, 0xe0
	ds_write_b64 v67, v[2:3] offset:0x4000
	v_add_u32_e32 v201, v32, v36
	v_xad_u32 v202, v36, 32, v32
	v_xad_u32 v203, v36, 64, v32
	v_xad_u32 v208, v36, s16, v32
	v_lshl_add_u32 v32, v143, 7, s10
	s_add_u32 s10, s78, 0x20000
	global_load_dwordx4 v[132:135], v198, s[8:9]
	s_addc_u32 s11, s79, 0
	global_load_dwordx4 v[128:131], v199, s[8:9]
	v_lshrrev_b32_e32 v34, 1, v137
	global_load_dwordx4 v[136:139], v196, s[10:11]
	s_add_u32 s6, s6, 0x180
	v_bitop3_b32 v34, v140, v34, 7 bitop3:0x78
	v_bitop3_b32 v37, v140, v35, 2 bitop3:0x36
	v_bitop3_b32 v38, v140, v35, 4 bitop3:0x36
	v_bitop3_b32 v35, v140, v35, 6 bitop3:0x36
	global_load_dwordx4 v[140:143], v197, s[10:11]
	s_addc_u32 s7, s7, 0
	s_add_u32 s8, s78, 0x30000
	global_load_dwordx4 v[148:151], v198, s[6:7]
	s_addc_u32 s9, s79, 0
	global_load_dwordx4 v[144:147], v199, s[6:7]
	global_load_dwordx4 v[152:155], v196, s[8:9]
	s_add_u32 s10, s13, s14
	global_load_dwordx4 v[156:159], v197, s[8:9]
	s_addc_u32 s11, s12, 0
	s_add_u32 s12, s41, s30
	v_mov_b32_e32 v0, 0
	s_mov_b32 s4, 0
	v_lshl_add_u32 v209, v34, 4, v32
	v_lshl_add_u32 v210, v37, 4, v32
	v_lshl_add_u32 v211, v38, 4, v32
	v_lshl_add_u32 v224, v35, 4, v32
	s_addc_u32 s13, 0, s31
	v_mov_b32_e32 v1, v0
	v_mov_b32_e32 v2, v0
	v_mov_b32_e32 v3, v0
	v_mov_b32_e32 v4, v0
	v_mov_b32_e32 v5, v0
	v_mov_b32_e32 v6, v0
	v_mov_b32_e32 v7, v0
	v_mov_b32_e32 v8, v0
	v_mov_b32_e32 v9, v0
	v_mov_b32_e32 v10, v0
	v_mov_b32_e32 v11, v0
	v_mov_b32_e32 v12, v0
	v_mov_b32_e32 v13, v0
	v_mov_b32_e32 v14, v0
	v_mov_b32_e32 v15, v0
	v_mov_b32_e32 v16, v0
	v_mov_b32_e32 v17, v0
	v_mov_b32_e32 v18, v0
	v_mov_b32_e32 v19, v0
	v_mov_b32_e32 v20, v0
	v_mov_b32_e32 v21, v0
	v_mov_b32_e32 v22, v0
	v_mov_b32_e32 v23, v0
	v_mov_b32_e32 v24, v0
	v_mov_b32_e32 v25, v0
	v_mov_b32_e32 v26, v0
	v_mov_b32_e32 v27, v0
	v_mov_b32_e32 v28, v0
	v_mov_b32_e32 v29, v0
	v_mov_b32_e32 v30, v0
	v_mov_b32_e32 v31, v0
	v_mov_b32_e32 v32, v0
	v_mov_b32_e32 v33, v0
	v_mov_b32_e32 v34, v0
	v_mov_b32_e32 v35, v0
	v_mov_b32_e32 v36, v0
	v_mov_b32_e32 v37, v0
	v_mov_b32_e32 v38, v0
	v_mov_b32_e32 v39, v0
	v_mov_b32_e32 v40, v0
	v_mov_b32_e32 v41, v0
	v_mov_b32_e32 v42, v0
	v_mov_b32_e32 v43, v0
	v_mov_b32_e32 v44, v0
	v_mov_b32_e32 v45, v0
	v_mov_b32_e32 v46, v0
	v_mov_b32_e32 v47, v0
	v_mov_b32_e32 v48, v0
	v_mov_b32_e32 v49, v0
	v_mov_b32_e32 v50, v0
	v_mov_b32_e32 v51, v0
	v_mov_b32_e32 v52, v0
	v_mov_b32_e32 v53, v0
	v_mov_b32_e32 v54, v0
	v_mov_b32_e32 v55, v0
	v_mov_b32_e32 v56, v0
	v_mov_b32_e32 v57, v0
	v_mov_b32_e32 v58, v0
	v_mov_b32_e32 v59, v0
	v_mov_b32_e32 v60, v0
	v_mov_b32_e32 v61, v0
	v_mov_b32_e32 v62, v0
	v_mov_b32_e32 v63, v0
	v_mov_b32_e32 v160, v0
	v_mov_b32_e32 v161, v0
	v_mov_b32_e32 v227, v64
	v_mov_b32_e32 v228, v65
	v_mov_b32_e32 v229, v66
	v_mov_b32_e32 v184, v67
	v_readlane_b32 s100, v250, 8
	v_mbcnt_lo_u32_b32 v68, -1, 0
	v_mbcnt_hi_u32_b32 v68, -1, v68
	v_and_b32_e32 v69, 15, v68
	v_lshrrev_b32_e32 v70, 4, v68
	v_lshlrev_b32_e32 v72, 8, v69
	v_add_u32_e32 v72, 0x10000, v72
	v_add_u32_e32 v71, 0, v70
	v_xor_b32_e32 v71, v71, v69
	v_lshl_add_u32 v201, v71, 4, v72
	v_add_u32_e32 v71, 4, v70
	v_xor_b32_e32 v71, v71, v69
	v_lshl_add_u32 v202, v71, 4, v72
	v_add_u32_e32 v71, 8, v70
	v_xor_b32_e32 v71, v71, v69
	v_lshl_add_u32 v203, v71, 4, v72
	v_add_u32_e32 v71, 12, v70
	v_xor_b32_e32 v71, v71, v69
	v_lshl_add_u32 v246, v71, 4, v72
	v_bfe_u32 v73, v69, 1, 3
	v_lshlrev_b32_e32 v76, 7, v69
	v_add_u32_e32 v71, 0, v70
	v_xor_b32_e32 v71, v71, v73
	v_lshl_add_u32 v209, v71, 4, v76
	v_add_u32_e32 v71, 4, v70
	v_xor_b32_e32 v71, v71, v73
	v_lshl_add_u32 v210, v71, 4, v76
	s_lshl_b32 s101, s100, 7
	s_add_u32 s101, s101, 0x8000
	s_cmpk_ge_u32 s100, 0x100
	s_cselect_b32 s6, 0x8000, 0
	s_add_u32 s101, s101, s6
	v_and_b32_e32 v74, 31, v68
	v_lshrrev_b32_e32 v75, 5, v68
	v_lshlrev_b32_e32 v74, 8, v74
	v_lshl_add_u32 v74, v75, 4, v74
	v_add_u32_e32 v74, s101, v74
	v_lshlrev_b32_e32 v75, 8, v69
	v_lshl_add_u32 v75, v70, 4, v75
	v_add_u32_e32 v75, s101, v75
	ds_write_b128 v74, v[96:99] offset:0
	ds_write_b128 v74, v[100:103] offset:32
	ds_write_b128 v74, v[104:107] offset:64
	ds_write_b128 v74, v[108:111] offset:96
	ds_write_b128 v74, v[112:115] offset:128
	ds_write_b128 v74, v[116:119] offset:160
	ds_write_b128 v74, v[120:123] offset:192
	ds_write_b128 v74, v[124:127] offset:224
	s_waitcnt lgkmcnt(0)
	ds_read_b128 v[96:99], v75 offset:0
	ds_read_b128 v[100:103], v75 offset:64
	ds_read_b128 v[104:107], v75 offset:128
	ds_read_b128 v[108:111], v75 offset:192
	ds_read_b128 v[112:115], v75 offset:4096
	ds_read_b128 v[116:119], v75 offset:4160
	ds_read_b128 v[120:123], v75 offset:4224
	ds_read_b128 v[124:127], v75 offset:4288
	s_waitcnt vmcnt(0)
	s_waitcnt lgkmcnt(0)
	s_barrier
	ds_write_b128 v225, v[136:139] offset:32768
	ds_write_b128 v226, v[140:143] offset:32768
	s_add_u32 s15, s22, s12
	s_addc_u32 s14, s23, s13
	s_add_u32 s6, s15, 0x23a40000
	s_addc_u32 s7, s14, 0
	s_waitcnt lgkmcnt(0)
	global_load_dwordx4 v[136:139], v196, s[6:7]
	global_load_dwordx4 v[140:143], v197, s[6:7]
	v_mov_b32_e32 v194, 0
	v_mov_b32_e32 v195, 0
	s_barrier
	s_cmpk_ge_u32 s100, 0x100
	s_cselect_b32 s100, 1, 0
	ds_read_b128 v[160:163], v201 offset:0
	ds_read_b128 v[164:167], v202 offset:0
	ds_read_b128 v[168:171], v203 offset:0
	ds_read_b128 v[172:175], v246 offset:0
	ds_read_b128 v[176:179], v201 offset:4096
	ds_read_b128 v[180:183], v202 offset:4096
	ds_read_b128 v[230:233], v203 offset:4096
	s_waitcnt lgkmcnt(6)
	v_mfma_f32_16x16x32_bf16 v[64:67], v[160:163], v[96:99], 0
	v_mfma_f32_16x16x32_bf16 v[68:71], v[160:163], v[112:115], 0
	ds_read_b128 v[234:237], v246 offset:4096
	s_waitcnt lgkmcnt(6)
	v_mfma_f32_16x16x32_bf16 v[68:71], v[164:167], v[116:119], v[68:71]
	v_mfma_f32_16x16x32_bf16 v[64:67], v[164:167], v[100:103], v[64:67]
	ds_read_b128 v[160:163], v201 offset:8192
	s_waitcnt lgkmcnt(6)
	v_mfma_f32_16x16x32_bf16 v[64:67], v[168:171], v[104:107], v[64:67]
	v_mfma_f32_16x16x32_bf16 v[68:71], v[168:171], v[120:123], v[68:71]
	ds_read_b128 v[164:167], v202 offset:8192
	s_waitcnt lgkmcnt(6)
	v_mfma_f32_16x16x32_bf16 v[68:71], v[172:175], v[124:127], v[68:71]
	v_mfma_f32_16x16x32_bf16 v[64:67], v[172:175], v[108:111], v[64:67]
	ds_read_b128 v[168:171], v203 offset:8192
	s_waitcnt lgkmcnt(6)
	v_mfma_f32_16x16x32_bf16 v[72:75], v[176:179], v[96:99], 0
	s_nop 7
	s_nop 1
	v_exp_f32_e32 v64, v64
	v_mfma_f32_16x16x32_bf16 v[76:79], v[176:179], v[112:115], 0
	v_exp_f32_e32 v68, v68
	ds_read_b128 v[172:175], v246 offset:8192
	s_waitcnt lgkmcnt(6)
	v_mfma_f32_16x16x32_bf16 v[76:79], v[180:183], v[116:119], v[76:79]
	v_exp_f32_e32 v65, v65
	v_exp_f32_e32 v69, v69
	v_mfma_f32_16x16x32_bf16 v[72:75], v[180:183], v[100:103], v[72:75]
	v_exp_f32_e32 v66, v66
	ds_read_b128 v[176:179], v201 offset:12288
	s_waitcnt lgkmcnt(6)
	v_mfma_f32_16x16x32_bf16 v[72:75], v[230:233], v[104:107], v[72:75]
	v_exp_f32_e32 v70, v70
	v_exp_f32_e32 v67, v67
	v_mfma_f32_16x16x32_bf16 v[76:79], v[230:233], v[120:123], v[76:79]
	v_exp_f32_e32 v71, v71
	v_add_f32_e32 v220, v64, v65
	ds_read_b128 v[180:183], v202 offset:12288
	s_waitcnt lgkmcnt(6)
	v_mfma_f32_16x16x32_bf16 v[76:79], v[234:237], v[124:127], v[76:79]
	v_add_f32_e32 v221, v68, v69
	v_add_f32_e32 v220, v220, v66
	v_add_f32_e32 v221, v221, v70
	v_mfma_f32_16x16x32_bf16 v[72:75], v[234:237], v[108:111], v[72:75]
	v_add_f32_e32 v220, v220, v67
	v_add_f32_e32 v221, v221, v71
	ds_read_b128 v[230:233], v203 offset:12288
	s_waitcnt lgkmcnt(6)
	v_mfma_f32_16x16x32_bf16 v[80:83], v[160:163], v[96:99], 0
	s_nop 7
	s_nop 1
	v_exp_f32_e32 v72, v72
	v_exp_f32_e32 v76, v76
	v_mfma_f32_16x16x32_bf16 v[84:87], v[160:163], v[112:115], 0
	v_exp_f32_e32 v73, v73
	v_exp_f32_e32 v77, v77
	ds_read_b128 v[234:237], v246 offset:12288
	s_waitcnt lgkmcnt(6)
	v_mfma_f32_16x16x32_bf16 v[84:87], v[164:167], v[116:119], v[84:87]
	v_exp_f32_e32 v74, v74
	v_exp_f32_e32 v78, v78
	v_mfma_f32_16x16x32_bf16 v[80:83], v[164:167], v[100:103], v[80:83]
	v_exp_f32_e32 v75, v75
	v_exp_f32_e32 v79, v79
	s_waitcnt lgkmcnt(5)
	v_mfma_f32_16x16x32_bf16 v[80:83], v[168:171], v[104:107], v[80:83]
	v_add_f32_e32 v220, v220, v72
	v_add_f32_e32 v221, v221, v76
	v_add_f32_e32 v220, v220, v73
	v_add_f32_e32 v221, v221, v77
	v_mfma_f32_16x16x32_bf16 v[84:87], v[168:171], v[120:123], v[84:87]
	v_add_f32_e32 v220, v220, v74
	v_add_f32_e32 v221, v221, v78
	v_add_f32_e32 v220, v220, v75
	v_add_f32_e32 v221, v221, v79
	s_waitcnt lgkmcnt(4)
	v_mfma_f32_16x16x32_bf16 v[84:87], v[172:175], v[124:127], v[84:87]
	v_cvt_pk_bf16_f32 v216, v64, v65
	v_cvt_pk_bf16_f32 v217, v66, v67
	v_cvt_pk_bf16_f32 v238, v68, v69
	v_cvt_pk_bf16_f32 v239, v70, v71
	v_mfma_f32_16x16x32_bf16 v[80:83], v[172:175], v[108:111], v[80:83]
	v_cvt_pk_bf16_f32 v218, v72, v73
	v_cvt_pk_bf16_f32 v219, v74, v75
	v_cvt_pk_bf16_f32 v240, v76, v77
	v_cvt_pk_bf16_f32 v241, v78, v79
	s_waitcnt lgkmcnt(3)
	v_mfma_f32_16x16x32_bf16 v[88:91], v[176:179], v[96:99], 0
	s_nop 7
	s_nop 1
	v_exp_f32_e32 v80, v80
	v_exp_f32_e32 v84, v84
	v_mfma_f32_16x16x32_bf16 v[92:95], v[176:179], v[112:115], 0
	v_exp_f32_e32 v81, v81
	s_waitcnt lgkmcnt(2)
	v_mfma_f32_16x16x32_bf16 v[92:95], v[180:183], v[116:119], v[92:95]
	v_exp_f32_e32 v85, v85
	v_exp_f32_e32 v82, v82
	v_mfma_f32_16x16x32_bf16 v[88:91], v[180:183], v[100:103], v[88:91]
	v_exp_f32_e32 v86, v86
	s_waitcnt lgkmcnt(1)
	v_mfma_f32_16x16x32_bf16 v[88:91], v[230:233], v[104:107], v[88:91]
	v_exp_f32_e32 v83, v83
	v_exp_f32_e32 v87, v87
	v_mfma_f32_16x16x32_bf16 v[92:95], v[230:233], v[120:123], v[92:95]
	v_add_f32_e32 v220, v220, v80
	v_add_f32_e32 v221, v221, v84
	v_add_f32_e32 v220, v220, v81
	s_waitcnt lgkmcnt(0)
	v_mfma_f32_16x16x32_bf16 v[92:95], v[234:237], v[124:127], v[92:95]
	v_add_f32_e32 v221, v221, v85
	v_add_f32_e32 v220, v220, v82
	v_add_f32_e32 v221, v221, v86
	v_mfma_f32_16x16x32_bf16 v[88:91], v[234:237], v[108:111], v[88:91]
	v_add_f32_e32 v220, v220, v83
	v_add_f32_e32 v221, v221, v87
	s_waitcnt lgkmcnt(0)
	s_barrier
	ds_read_b128 v[160:163], v201 offset:16384
	ds_read_b128 v[164:167], v209 offset:0
	ds_read_b128 v[168:171], v202 offset:16384
	ds_read_b128 v[172:175], v209 offset:2048
	ds_read_b128 v[176:179], v203 offset:16384
	ds_read_b128 v[180:183], v209 offset:4096
	ds_read_b128 v[230:233], v246 offset:16384
.LBB0_734:
	s_cmp_eq_u32 s100, 0
	s_cbranch_scc1 .Lattn_pa0
	s_setprio 1
	s_branch .Lattn_pb0

.Lattn_pb1:
	s_waitcnt lgkmcnt(6)
	v_mfma_f32_16x16x32_bf16 v[64:67], v[160:163], v[96:99], 0
	v_exp_f32_e32 v88, v88
	v_mfma_f32_16x16x32_bf16 v[68:71], v[160:163], v[112:115], 0
	v_exp_f32_e32 v92, v92
	ds_read_b128 v[234:237], v209 offset:22528
	s_add_u32 s8, s16, 0x3bc00280
	s_addc_u32 s9, s17, 0
	s_add_u32 s6, s15, 0x23a60000
	s_addc_u32 s7, s14, 0
	s_waitcnt lgkmcnt(6)
	v_mfma_f32_16x16x32_bf16 v[0:3], v[164:167], v[216:219], v[0:3]
	v_cvt_pk_bf16_f32 v242, v80, v81
	v_mfma_f32_16x16x32_bf16 v[4:7], v[164:167], v[238:241], v[4:7]
	v_exp_f32_e32 v89, v89
	ds_read_b128 v[160:163], v201 offset:36864
	s_waitcnt vmcnt(4)
	ds_write_b128 v225, v[136:139] offset:0
	s_waitcnt lgkmcnt(7)
	v_mfma_f32_16x16x32_bf16 v[68:71], v[168:171], v[116:119], v[68:71]
	v_exp_f32_e32 v93, v93
	v_mfma_f32_16x16x32_bf16 v[64:67], v[168:171], v[100:103], v[64:67]
	v_cvt_pk_bf16_f32 v243, v82, v83
	ds_read_b128 v[164:167], v209 offset:24576
	ds_write_b128 v226, v[140:143] offset:0
	s_waitcnt lgkmcnt(8)
	v_mfma_f32_16x16x32_bf16 v[12:15], v[172:175], v[238:241], v[12:15]
	v_exp_f32_e32 v90, v90
	v_mfma_f32_16x16x32_bf16 v[8:11], v[172:175], v[216:219], v[8:11]
	v_exp_f32_e32 v94, v94
	ds_read_b128 v[168:171], v202 offset:36864
	ds_write_b64 v227, v[148:149] offset:49152
	s_waitcnt lgkmcnt(9)
	v_mfma_f32_16x16x32_bf16 v[64:67], v[176:179], v[104:107], v[64:67]
	v_cvt_pk_bf16_f32 v204, v84, v85
	v_mfma_f32_16x16x32_bf16 v[68:71], v[176:179], v[120:123], v[68:71]
	v_exp_f32_e32 v91, v91
	ds_read_b128 v[172:175], v209 offset:26624
	ds_write_b64 v228, v[150:151] offset:49152
	s_waitcnt lgkmcnt(10)
	v_mfma_f32_16x16x32_bf16 v[16:19], v[180:183], v[216:219], v[16:19]
	v_exp_f32_e32 v95, v95
	v_mfma_f32_16x16x32_bf16 v[20:23], v[180:183], v[238:241], v[20:23]
	v_cvt_pk_bf16_f32 v205, v86, v87
	v_add_f32_e32 v220, v220, v88
	ds_read_b128 v[176:179], v203 offset:36864
	ds_write_b64 v229, v[144:145] offset:49152
	s_waitcnt lgkmcnt(11)
	v_mfma_f32_16x16x32_bf16 v[68:71], v[230:233], v[124:127], v[68:71]
	v_add_f32_e32 v221, v221, v92
	v_add_f32_e32 v220, v220, v89
	v_mfma_f32_16x16x32_bf16 v[64:67], v[230:233], v[108:111], v[64:67]
	v_add_f32_e32 v221, v221, v93
	v_cvt_pk_bf16_f32 v244, v88, v89
	ds_read_b128 v[180:183], v209 offset:28672
	ds_write_b64 v184, v[146:147] offset:49152
	s_waitcnt lgkmcnt(12)
	v_mfma_f32_16x16x32_bf16 v[28:31], v[234:237], v[238:241], v[28:31]
	v_cvt_pk_bf16_f32 v245, v90, v91
	v_cvt_pk_bf16_f32 v206, v92, v93
	v_mfma_f32_16x16x32_bf16 v[24:27], v[234:237], v[216:219], v[24:27]
	v_cvt_pk_bf16_f32 v207, v94, v95
	ds_read_b128 v[230:233], v246 offset:36864
	global_load_dwordx4 v[148:151], v198, s[8:9]
	s_waitcnt lgkmcnt(12)
	v_mfma_f32_16x16x32_bf16 v[72:75], v[160:163], v[96:99], 0
	v_add_f32_e32 v220, v220, v90
	v_add_f32_e32 v221, v221, v94
	v_mfma_f32_16x16x32_bf16 v[76:79], v[160:163], v[112:115], 0
	v_add_f32_e32 v220, v220, v91
	v_add_f32_e32 v221, v221, v95
	ds_read_b128 v[234:237], v209 offset:30720
	global_load_dwordx4 v[144:147], v199, s[8:9]
	s_waitcnt lgkmcnt(11)
	v_mfma_f32_16x16x32_bf16 v[32:35], v[164:167], v[216:219], v[32:35]
	v_add_f32_e32 v194, v194, v220
	v_add_f32_e32 v195, v195, v221
	v_mfma_f32_16x16x32_bf16 v[36:39], v[164:167], v[238:241], v[36:39]
	v_exp_f32_e32 v64, v64
	ds_read_b128 v[160:163], v201 offset:40960
	global_load_dwordx4 v[136:139], v196, s[6:7]
	s_waitcnt lgkmcnt(10)
	v_mfma_f32_16x16x32_bf16 v[76:79], v[168:171], v[116:119], v[76:79]
	v_exp_f32_e32 v68, v68
	v_mfma_f32_16x16x32_bf16 v[72:75], v[168:171], v[100:103], v[72:75]
	v_exp_f32_e32 v65, v65
	ds_read_b128 v[164:167], v210 offset:16384
	global_load_dwordx4 v[140:143], v197, s[6:7]
	s_waitcnt lgkmcnt(9)
	v_mfma_f32_16x16x32_bf16 v[44:47], v[172:175], v[238:241], v[44:47]
	v_exp_f32_e32 v69, v69
	v_mfma_f32_16x16x32_bf16 v[40:43], v[172:175], v[216:219], v[40:43]
	v_exp_f32_e32 v66, v66
	ds_read_b128 v[168:171], v202 offset:40960
	s_waitcnt lgkmcnt(8)
	v_mfma_f32_16x16x32_bf16 v[72:75], v[176:179], v[104:107], v[72:75]
	v_exp_f32_e32 v70, v70
	v_mfma_f32_16x16x32_bf16 v[76:79], v[176:179], v[120:123], v[76:79]
	v_exp_f32_e32 v67, v67
	ds_read_b128 v[172:175], v210 offset:18432
	s_waitcnt lgkmcnt(7)
	v_mfma_f32_16x16x32_bf16 v[48:51], v[180:183], v[216:219], v[48:51]
	v_exp_f32_e32 v71, v71
	v_mfma_f32_16x16x32_bf16 v[52:55], v[180:183], v[238:241], v[52:55]
	v_add_f32_e32 v220, v64, v65
	ds_read_b128 v[176:179], v203 offset:40960
	s_waitcnt lgkmcnt(6)
	v_mfma_f32_16x16x32_bf16 v[76:79], v[230:233], v[124:127], v[76:79]
	v_add_f32_e32 v221, v68, v69
	v_mfma_f32_16x16x32_bf16 v[72:75], v[230:233], v[108:111], v[72:75]
	v_add_f32_e32 v220, v220, v66
	ds_read_b128 v[180:183], v210 offset:20480
	s_waitcnt lgkmcnt(6)
	v_mfma_f32_16x16x32_bf16 v[60:63], v[234:237], v[238:241], v[60:63]
	v_add_f32_e32 v221, v221, v70
	v_add_f32_e32 v220, v220, v67
	v_mfma_f32_16x16x32_bf16 v[56:59], v[234:237], v[216:219], v[56:59]
	v_add_f32_e32 v221, v221, v71
	ds_read_b128 v[230:233], v246 offset:40960
	s_waitcnt lgkmcnt(6)
	v_mfma_f32_16x16x32_bf16 v[80:83], v[160:163], v[96:99], 0
	v_exp_f32_e32 v72, v72
	v_mfma_f32_16x16x32_bf16 v[84:87], v[160:163], v[112:115], 0
	v_exp_f32_e32 v76, v76
	ds_read_b128 v[234:237], v210 offset:22528
	s_waitcnt lgkmcnt(6)
	v_mfma_f32_16x16x32_bf16 v[0:3], v[164:167], v[242:245], v[0:3]
	v_exp_f32_e32 v73, v73
	v_mfma_f32_16x16x32_bf16 v[4:7], v[164:167], v[204:207], v[4:7]
	v_exp_f32_e32 v77, v77
	ds_read_b128 v[160:163], v201 offset:45056
	s_waitcnt lgkmcnt(6)
	v_mfma_f32_16x16x32_bf16 v[84:87], v[168:171], v[116:119], v[84:87]
	v_exp_f32_e32 v74, v74
	v_mfma_f32_16x16x32_bf16 v[80:83], v[168:171], v[100:103], v[80:83]
	v_exp_f32_e32 v78, v78
	ds_read_b128 v[164:167], v210 offset:24576
	s_waitcnt lgkmcnt(6)
	v_mfma_f32_16x16x32_bf16 v[12:15], v[172:175], v[204:207], v[12:15]
	v_exp_f32_e32 v75, v75
	v_mfma_f32_16x16x32_bf16 v[8:11], v[172:175], v[242:245], v[8:11]
	v_exp_f32_e32 v79, v79
	ds_read_b128 v[168:171], v202 offset:45056
	s_waitcnt lgkmcnt(6)
	v_mfma_f32_16x16x32_bf16 v[80:83], v[176:179], v[104:107], v[80:83]
	v_add_f32_e32 v220, v220, v72
	v_add_f32_e32 v221, v221, v76
	v_mfma_f32_16x16x32_bf16 v[84:87], v[176:179], v[120:123], v[84:87]
	v_add_f32_e32 v220, v220, v73
	ds_read_b128 v[172:175], v210 offset:26624
	s_waitcnt lgkmcnt(6)
	v_mfma_f32_16x16x32_bf16 v[16:19], v[180:183], v[242:245], v[16:19]
	v_add_f32_e32 v221, v221, v77
	v_add_f32_e32 v220, v220, v74
	v_mfma_f32_16x16x32_bf16 v[20:23], v[180:183], v[204:207], v[20:23]
	v_add_f32_e32 v221, v221, v78
	ds_read_b128 v[176:179], v203 offset:45056
	s_waitcnt lgkmcnt(6)
	v_mfma_f32_16x16x32_bf16 v[84:87], v[230:233], v[124:127], v[84:87]
	v_add_f32_e32 v220, v220, v75
	v_add_f32_e32 v221, v221, v79
	v_mfma_f32_16x16x32_bf16 v[80:83], v[230:233], v[108:111], v[80:83]
	v_cvt_pk_bf16_f32 v216, v64, v65
	ds_read_b128 v[180:183], v210 offset:28672
	s_waitcnt lgkmcnt(6)
	v_mfma_f32_16x16x32_bf16 v[28:31], v[234:237], v[204:207], v[28:31]
	v_cvt_pk_bf16_f32 v217, v66, v67
	v_cvt_pk_bf16_f32 v238, v68, v69
	v_mfma_f32_16x16x32_bf16 v[24:27], v[234:237], v[242:245], v[24:27]
	v_cvt_pk_bf16_f32 v239, v70, v71
	ds_read_b128 v[230:233], v246 offset:45056
	s_waitcnt lgkmcnt(6)
	v_mfma_f32_16x16x32_bf16 v[88:91], v[160:163], v[96:99], 0
	v_exp_f32_e32 v80, v80
	v_mfma_f32_16x16x32_bf16 v[92:95], v[160:163], v[112:115], 0
	v_exp_f32_e32 v84, v84
	ds_read_b128 v[234:237], v210 offset:30720
	s_waitcnt lgkmcnt(6)
	v_mfma_f32_16x16x32_bf16 v[32:35], v[164:167], v[242:245], v[32:35]
	v_exp_f32_e32 v81, v81
	v_mfma_f32_16x16x32_bf16 v[36:39], v[164:167], v[204:207], v[36:39]
	v_exp_f32_e32 v85, v85
	s_waitcnt lgkmcnt(5)
	v_mfma_f32_16x16x32_bf16 v[92:95], v[168:171], v[116:119], v[92:95]
	v_exp_f32_e32 v82, v82
	v_mfma_f32_16x16x32_bf16 v[88:91], v[168:171], v[100:103], v[88:91]
	v_exp_f32_e32 v86, v86
	s_waitcnt lgkmcnt(4)
	v_mfma_f32_16x16x32_bf16 v[44:47], v[172:175], v[204:207], v[44:47]
	v_exp_f32_e32 v83, v83
	v_mfma_f32_16x16x32_bf16 v[40:43], v[172:175], v[242:245], v[40:43]
	v_exp_f32_e32 v87, v87
	s_waitcnt lgkmcnt(3)
	v_mfma_f32_16x16x32_bf16 v[88:91], v[176:179], v[104:107], v[88:91]
	v_add_f32_e32 v220, v220, v80
	v_add_f32_e32 v221, v221, v84
	v_mfma_f32_16x16x32_bf16 v[92:95], v[176:179], v[120:123], v[92:95]
	v_add_f32_e32 v220, v220, v81
	s_waitcnt lgkmcnt(0)
	s_barrier
	ds_read_b128 v[160:163], v201 offset:49152
	ds_read_b128 v[164:167], v209 offset:32768
	ds_read_b128 v[168:171], v202 offset:49152
	ds_read_b128 v[172:175], v209 offset:34816
	v_mfma_f32_16x16x32_bf16 v[48:51], v[180:183], v[242:245], v[48:51]
	v_add_f32_e32 v221, v221, v85
	v_add_f32_e32 v220, v220, v82
	v_mfma_f32_16x16x32_bf16 v[52:55], v[180:183], v[204:207], v[52:55]
	v_add_f32_e32 v221, v221, v86
	ds_read_b128 v[176:179], v203 offset:49152
	v_mfma_f32_16x16x32_bf16 v[92:95], v[230:233], v[124:127], v[92:95]
	v_add_f32_e32 v220, v220, v83
	v_add_f32_e32 v221, v221, v87
	v_mfma_f32_16x16x32_bf16 v[88:91], v[230:233], v[108:111], v[88:91]
	v_cvt_pk_bf16_f32 v218, v72, v73
	ds_read_b128 v[180:183], v209 offset:36864
	v_mfma_f32_16x16x32_bf16 v[60:63], v[234:237], v[204:207], v[60:63]
	v_cvt_pk_bf16_f32 v219, v74, v75
	v_cvt_pk_bf16_f32 v240, v76, v77
	v_mfma_f32_16x16x32_bf16 v[56:59], v[234:237], v[242:245], v[56:59]
	v_cvt_pk_bf16_f32 v241, v78, v79
	ds_read_b128 v[230:233], v246 offset:49152
	s_cmp_eq_u32 s100, 0
	s_cbranch_scc1 .Lattn_pa2
	s_setprio 1
	s_branch .Lattn_pb2

.Lattn_pb3:
	s_waitcnt lgkmcnt(6)
	v_mfma_f32_16x16x32_bf16 v[64:67], v[160:163], v[96:99], 0
	v_exp_f32_e32 v88, v88
	v_mfma_f32_16x16x32_bf16 v[68:71], v[160:163], v[112:115], 0
	v_exp_f32_e32 v92, v92
	ds_read_b128 v[234:237], v209 offset:55296
	s_add_u32 s8, s16, 0x3bc00380
	s_addc_u32 s9, s17, 0
	s_add_u32 s6, s15, 0x23a80000
	s_addc_u32 s7, s14, 0
	s_waitcnt lgkmcnt(6)
	v_mfma_f32_16x16x32_bf16 v[0:3], v[164:167], v[216:219], v[0:3]
	v_cvt_pk_bf16_f32 v242, v80, v81
	v_mfma_f32_16x16x32_bf16 v[4:7], v[164:167], v[238:241], v[4:7]
	v_exp_f32_e32 v89, v89
	ds_read_b128 v[160:163], v201 offset:4096
	s_waitcnt vmcnt(4)
	ds_write_b128 v225, v[136:139] offset:32768
	s_waitcnt lgkmcnt(7)
	v_mfma_f32_16x16x32_bf16 v[68:71], v[168:171], v[116:119], v[68:71]
	v_exp_f32_e32 v93, v93
	v_mfma_f32_16x16x32_bf16 v[64:67], v[168:171], v[100:103], v[64:67]
	v_cvt_pk_bf16_f32 v243, v82, v83
	ds_read_b128 v[164:167], v209 offset:57344
	ds_write_b128 v226, v[140:143] offset:32768
	s_waitcnt lgkmcnt(8)
	v_mfma_f32_16x16x32_bf16 v[12:15], v[172:175], v[238:241], v[12:15]
	v_exp_f32_e32 v90, v90
	v_mfma_f32_16x16x32_bf16 v[8:11], v[172:175], v[216:219], v[8:11]
	v_exp_f32_e32 v94, v94
	ds_read_b128 v[168:171], v202 offset:4096
	ds_write_b64 v227, v[148:149] offset:16384
	s_waitcnt lgkmcnt(9)
	v_mfma_f32_16x16x32_bf16 v[64:67], v[176:179], v[104:107], v[64:67]
	v_cvt_pk_bf16_f32 v204, v84, v85
	v_mfma_f32_16x16x32_bf16 v[68:71], v[176:179], v[120:123], v[68:71]
	v_exp_f32_e32 v91, v91
	ds_read_b128 v[172:175], v209 offset:59392
	ds_write_b64 v228, v[150:151] offset:16384
	s_waitcnt lgkmcnt(10)
	v_mfma_f32_16x16x32_bf16 v[16:19], v[180:183], v[216:219], v[16:19]
	v_exp_f32_e32 v95, v95
	v_mfma_f32_16x16x32_bf16 v[20:23], v[180:183], v[238:241], v[20:23]
	v_cvt_pk_bf16_f32 v205, v86, v87
	v_add_f32_e32 v220, v220, v88
	ds_read_b128 v[176:179], v203 offset:4096
	ds_write_b64 v229, v[144:145] offset:16384
	s_waitcnt lgkmcnt(11)
	v_mfma_f32_16x16x32_bf16 v[68:71], v[230:233], v[124:127], v[68:71]
	v_add_f32_e32 v221, v221, v92
	v_add_f32_e32 v220, v220, v89
	v_mfma_f32_16x16x32_bf16 v[64:67], v[230:233], v[108:111], v[64:67]
	v_add_f32_e32 v221, v221, v93
	v_cvt_pk_bf16_f32 v244, v88, v89
	ds_read_b128 v[180:183], v209 offset:61440
	ds_write_b64 v184, v[146:147] offset:16384
	s_waitcnt lgkmcnt(12)
	v_mfma_f32_16x16x32_bf16 v[28:31], v[234:237], v[238:241], v[28:31]
	v_cvt_pk_bf16_f32 v245, v90, v91
	v_cvt_pk_bf16_f32 v206, v92, v93
	v_mfma_f32_16x16x32_bf16 v[24:27], v[234:237], v[216:219], v[24:27]
	v_cvt_pk_bf16_f32 v207, v94, v95
	ds_read_b128 v[230:233], v246 offset:4096
	global_load_dwordx4 v[148:151], v198, s[8:9]
	s_waitcnt lgkmcnt(12)
	v_mfma_f32_16x16x32_bf16 v[72:75], v[160:163], v[96:99], 0
	v_add_f32_e32 v220, v220, v90
	v_add_f32_e32 v221, v221, v94
	v_mfma_f32_16x16x32_bf16 v[76:79], v[160:163], v[112:115], 0
	v_add_f32_e32 v220, v220, v91
	v_add_f32_e32 v221, v221, v95
	ds_read_b128 v[234:237], v209 offset:63488
	global_load_dwordx4 v[144:147], v199, s[8:9]
	s_waitcnt lgkmcnt(11)
	v_mfma_f32_16x16x32_bf16 v[32:35], v[164:167], v[216:219], v[32:35]
	v_add_f32_e32 v194, v194, v220
	v_add_f32_e32 v195, v195, v221
	v_mfma_f32_16x16x32_bf16 v[36:39], v[164:167], v[238:241], v[36:39]
	v_exp_f32_e32 v64, v64
	ds_read_b128 v[160:163], v201 offset:8192
	global_load_dwordx4 v[136:139], v196, s[6:7]
	s_waitcnt lgkmcnt(10)
	v_mfma_f32_16x16x32_bf16 v[76:79], v[168:171], v[116:119], v[76:79]
	v_exp_f32_e32 v68, v68
	v_mfma_f32_16x16x32_bf16 v[72:75], v[168:171], v[100:103], v[72:75]
	v_exp_f32_e32 v65, v65
	ds_read_b128 v[164:167], v210 offset:49152
	global_load_dwordx4 v[140:143], v197, s[6:7]
	s_waitcnt lgkmcnt(9)
	v_mfma_f32_16x16x32_bf16 v[44:47], v[172:175], v[238:241], v[44:47]
	v_exp_f32_e32 v69, v69
	v_mfma_f32_16x16x32_bf16 v[40:43], v[172:175], v[216:219], v[40:43]
	v_exp_f32_e32 v66, v66
	ds_read_b128 v[168:171], v202 offset:8192
	s_waitcnt lgkmcnt(8)
	v_mfma_f32_16x16x32_bf16 v[72:75], v[176:179], v[104:107], v[72:75]
	v_exp_f32_e32 v70, v70
	v_mfma_f32_16x16x32_bf16 v[76:79], v[176:179], v[120:123], v[76:79]
	v_exp_f32_e32 v67, v67
	ds_read_b128 v[172:175], v210 offset:51200
	s_waitcnt lgkmcnt(7)
	v_mfma_f32_16x16x32_bf16 v[48:51], v[180:183], v[216:219], v[48:51]
	v_exp_f32_e32 v71, v71
	v_mfma_f32_16x16x32_bf16 v[52:55], v[180:183], v[238:241], v[52:55]
	v_add_f32_e32 v220, v64, v65
	ds_read_b128 v[176:179], v203 offset:8192
	s_waitcnt lgkmcnt(6)
	v_mfma_f32_16x16x32_bf16 v[76:79], v[230:233], v[124:127], v[76:79]
	v_add_f32_e32 v221, v68, v69
	v_mfma_f32_16x16x32_bf16 v[72:75], v[230:233], v[108:111], v[72:75]
	v_add_f32_e32 v220, v220, v66
	ds_read_b128 v[180:183], v210 offset:53248
	s_waitcnt lgkmcnt(6)
	v_mfma_f32_16x16x32_bf16 v[60:63], v[234:237], v[238:241], v[60:63]
	v_add_f32_e32 v221, v221, v70
	v_add_f32_e32 v220, v220, v67
	v_mfma_f32_16x16x32_bf16 v[56:59], v[234:237], v[216:219], v[56:59]
	v_add_f32_e32 v221, v221, v71
	ds_read_b128 v[230:233], v246 offset:8192
	s_waitcnt lgkmcnt(6)
	v_mfma_f32_16x16x32_bf16 v[80:83], v[160:163], v[96:99], 0
	v_exp_f32_e32 v72, v72
	v_mfma_f32_16x16x32_bf16 v[84:87], v[160:163], v[112:115], 0
	v_exp_f32_e32 v76, v76
	ds_read_b128 v[234:237], v210 offset:55296
	s_waitcnt lgkmcnt(6)
	v_mfma_f32_16x16x32_bf16 v[0:3], v[164:167], v[242:245], v[0:3]
	v_exp_f32_e32 v73, v73
	v_mfma_f32_16x16x32_bf16 v[4:7], v[164:167], v[204:207], v[4:7]
	v_exp_f32_e32 v77, v77
	ds_read_b128 v[160:163], v201 offset:12288
	s_waitcnt lgkmcnt(6)
	v_mfma_f32_16x16x32_bf16 v[84:87], v[168:171], v[116:119], v[84:87]
	v_exp_f32_e32 v74, v74
	v_mfma_f32_16x16x32_bf16 v[80:83], v[168:171], v[100:103], v[80:83]
	v_exp_f32_e32 v78, v78
	ds_read_b128 v[164:167], v210 offset:57344
	s_waitcnt lgkmcnt(6)
	v_mfma_f32_16x16x32_bf16 v[12:15], v[172:175], v[204:207], v[12:15]
	v_exp_f32_e32 v75, v75
	v_mfma_f32_16x16x32_bf16 v[8:11], v[172:175], v[242:245], v[8:11]
	v_exp_f32_e32 v79, v79
	ds_read_b128 v[168:171], v202 offset:12288
	s_waitcnt lgkmcnt(6)
	v_mfma_f32_16x16x32_bf16 v[80:83], v[176:179], v[104:107], v[80:83]
	v_add_f32_e32 v220, v220, v72
	v_add_f32_e32 v221, v221, v76
	v_mfma_f32_16x16x32_bf16 v[84:87], v[176:179], v[120:123], v[84:87]
	v_add_f32_e32 v220, v220, v73
	ds_read_b128 v[172:175], v210 offset:59392
	s_add_u32 s10, s10, 0x200
	s_addc_u32 s11, s11, 0
	s_add_u32 s12, s12, 0x40000
	s_addc_u32 s13, s13, 0
	s_add_i32 s4, s4, 4
	s_cmpk_lt_u32 s4, 0x104
	s_cselect_b64 s[6:7], -1, 0
	s_and_b64 s[6:7], s[0:1], s[6:7]
	s_and_b64 vcc, exec, s[6:7]
	s_waitcnt lgkmcnt(6)
	v_mfma_f32_16x16x32_bf16 v[16:19], v[180:183], v[242:245], v[16:19]
	v_add_f32_e32 v221, v221, v77
	v_add_f32_e32 v220, v220, v74
	v_mfma_f32_16x16x32_bf16 v[20:23], v[180:183], v[204:207], v[20:23]
	v_add_f32_e32 v221, v221, v78
	ds_read_b128 v[176:179], v203 offset:12288
	s_waitcnt lgkmcnt(6)
	v_mfma_f32_16x16x32_bf16 v[84:87], v[230:233], v[124:127], v[84:87]
	v_add_f32_e32 v220, v220, v75
	v_add_f32_e32 v221, v221, v79
	v_mfma_f32_16x16x32_bf16 v[80:83], v[230:233], v[108:111], v[80:83]
	v_cvt_pk_bf16_f32 v216, v64, v65
	ds_read_b128 v[180:183], v210 offset:61440
	s_waitcnt lgkmcnt(6)
	v_mfma_f32_16x16x32_bf16 v[28:31], v[234:237], v[204:207], v[28:31]
	v_cvt_pk_bf16_f32 v217, v66, v67
	v_cvt_pk_bf16_f32 v238, v68, v69
	v_mfma_f32_16x16x32_bf16 v[24:27], v[234:237], v[242:245], v[24:27]
	v_cvt_pk_bf16_f32 v239, v70, v71
	ds_read_b128 v[230:233], v246 offset:12288
	s_waitcnt lgkmcnt(6)
	v_mfma_f32_16x16x32_bf16 v[88:91], v[160:163], v[96:99], 0
	v_exp_f32_e32 v80, v80
	v_mfma_f32_16x16x32_bf16 v[92:95], v[160:163], v[112:115], 0
	v_exp_f32_e32 v84, v84
	ds_read_b128 v[234:237], v210 offset:63488
	s_waitcnt lgkmcnt(6)
	v_mfma_f32_16x16x32_bf16 v[32:35], v[164:167], v[242:245], v[32:35]
	v_exp_f32_e32 v81, v81
	v_mfma_f32_16x16x32_bf16 v[36:39], v[164:167], v[204:207], v[36:39]
	v_exp_f32_e32 v85, v85
	s_waitcnt lgkmcnt(5)
	v_mfma_f32_16x16x32_bf16 v[92:95], v[168:171], v[116:119], v[92:95]
	v_exp_f32_e32 v82, v82
	v_mfma_f32_16x16x32_bf16 v[88:91], v[168:171], v[100:103], v[88:91]
	v_exp_f32_e32 v86, v86
	s_waitcnt lgkmcnt(4)
	v_mfma_f32_16x16x32_bf16 v[44:47], v[172:175], v[204:207], v[44:47]
	v_exp_f32_e32 v83, v83
	v_mfma_f32_16x16x32_bf16 v[40:43], v[172:175], v[242:245], v[40:43]
	v_exp_f32_e32 v87, v87
	s_waitcnt lgkmcnt(3)
	v_mfma_f32_16x16x32_bf16 v[88:91], v[176:179], v[104:107], v[88:91]
	v_add_f32_e32 v220, v220, v80
	v_add_f32_e32 v221, v221, v84
	v_mfma_f32_16x16x32_bf16 v[92:95], v[176:179], v[120:123], v[92:95]
	v_add_f32_e32 v220, v220, v81
	s_waitcnt lgkmcnt(0)
	s_barrier
	ds_read_b128 v[160:163], v201 offset:16384
	ds_read_b128 v[164:167], v209 offset:0
	ds_read_b128 v[168:171], v202 offset:16384
	ds_read_b128 v[172:175], v209 offset:2048
	v_mfma_f32_16x16x32_bf16 v[48:51], v[180:183], v[242:245], v[48:51]
	v_add_f32_e32 v221, v221, v85
	v_add_f32_e32 v220, v220, v82
	v_mfma_f32_16x16x32_bf16 v[52:55], v[180:183], v[204:207], v[52:55]
	v_add_f32_e32 v221, v221, v86
	ds_read_b128 v[176:179], v203 offset:16384
	v_mfma_f32_16x16x32_bf16 v[92:95], v[230:233], v[124:127], v[92:95]
	v_add_f32_e32 v220, v220, v83
	v_add_f32_e32 v221, v221, v87
	v_mfma_f32_16x16x32_bf16 v[88:91], v[230:233], v[108:111], v[88:91]
	v_cvt_pk_bf16_f32 v218, v72, v73
	ds_read_b128 v[180:183], v209 offset:4096
	v_mfma_f32_16x16x32_bf16 v[60:63], v[234:237], v[204:207], v[60:63]
	v_cvt_pk_bf16_f32 v219, v74, v75
	v_cvt_pk_bf16_f32 v240, v76, v77
	v_mfma_f32_16x16x32_bf16 v[56:59], v[234:237], v[242:245], v[56:59]
	v_cvt_pk_bf16_f32 v241, v78, v79
	ds_read_b128 v[230:233], v246 offset:16384
	s_cbranch_vccnz .LBB0_734
	s_setprio 0
	s_waitcnt vmcnt(0)
	s_nop 7
	s_nop 7
	ds_swizzle_b32 v64, v194 offset:swizzle(SWAP,16)
	s_waitcnt lgkmcnt(0)
	v_add_f32_e32 v194, v194, v64
	v_mov_b32_e32 v65, v194
	s_nop 1
	v_permlane32_swap_b32_e32 v194, v65
	v_add_f32_e32 v194, v194, v65
	s_nop 0
	v_rcp_f32_e32 v66, v194
	ds_swizzle_b32 v64, v195 offset:swizzle(SWAP,16)
	s_waitcnt lgkmcnt(0)
	v_add_f32_e32 v195, v195, v64
	v_mov_b32_e32 v65, v195
	s_nop 1
	v_permlane32_swap_b32_e32 v195, v65
	v_add_f32_e32 v195, v195, v65
	s_nop 0
	v_rcp_f32_e32 v67, v195
	v_readlane_b32 s100, v250, 8
	v_mbcnt_lo_u32_b32 v68, -1, 0
	v_mbcnt_hi_u32_b32 v68, -1, v68
	v_and_b32_e32 v69, 15, v68
	v_lshrrev_b32_e32 v70, 4, v68
	s_lshr_b32 s101, s100, 1
	v_add_u32_e32 v69, s101, v69
	v_lshlrev_b32_e32 v69, 12, v69
	v_and_b32_e32 v71, 1, v70
	v_lshlrev_b32_e32 v71, 5, v71
	v_and_b32_e32 v70, 2, v70
	v_lshl_add_u32 v71, v70, 3, v71
	v_add_u32_e32 v70, v69, v71
	v_add_u32_e32 v71, 0x10000, v70
	v_mul_f32_e32 v0, v0, v66
	v_mul_f32_e32 v1, v1, v66
	v_mul_f32_e32 v2, v2, v66
	v_mul_f32_e32 v3, v3, v66
	v_mul_f32_e32 v8, v8, v66
	v_mul_f32_e32 v9, v9, v66
	v_mul_f32_e32 v10, v10, v66
	v_mul_f32_e32 v11, v11, v66
	v_cvt_pk_bf16_f32 v72, v0, v1
	v_cvt_pk_bf16_f32 v73, v2, v3
	v_cvt_pk_bf16_f32 v74, v8, v9
	v_cvt_pk_bf16_f32 v75, v10, v11
	s_nop 1
	v_permlane16_swap_b32_e32 v72, v74
	v_permlane16_swap_b32_e32 v73, v75
	s_nop 1
	global_store_dwordx4 v70, v[72:75], s[58:59] offset:0
	v_mul_f32_e32 v16, v16, v66
	v_mul_f32_e32 v17, v17, v66
	v_mul_f32_e32 v18, v18, v66
	v_mul_f32_e32 v19, v19, v66
	v_mul_f32_e32 v24, v24, v66
	v_mul_f32_e32 v25, v25, v66
	v_mul_f32_e32 v26, v26, v66
	v_mul_f32_e32 v27, v27, v66
	v_cvt_pk_bf16_f32 v76, v16, v17
	v_cvt_pk_bf16_f32 v77, v18, v19
	v_cvt_pk_bf16_f32 v78, v24, v25
	v_cvt_pk_bf16_f32 v79, v26, v27
	s_nop 1
	v_permlane16_swap_b32_e32 v76, v78
	v_permlane16_swap_b32_e32 v77, v79
	s_nop 1
	global_store_dwordx4 v70, v[76:79], s[58:59] offset:64
	v_mul_f32_e32 v32, v32, v66
	v_mul_f32_e32 v33, v33, v66
	v_mul_f32_e32 v34, v34, v66
	v_mul_f32_e32 v35, v35, v66
	v_mul_f32_e32 v40, v40, v66
	v_mul_f32_e32 v41, v41, v66
	v_mul_f32_e32 v42, v42, v66
	v_mul_f32_e32 v43, v43, v66
	v_cvt_pk_bf16_f32 v80, v32, v33
	v_cvt_pk_bf16_f32 v81, v34, v35
	v_cvt_pk_bf16_f32 v82, v40, v41
	v_cvt_pk_bf16_f32 v83, v42, v43
	s_nop 1
	v_permlane16_swap_b32_e32 v80, v82
	v_permlane16_swap_b32_e32 v81, v83
	s_nop 1
	global_store_dwordx4 v70, v[80:83], s[58:59] offset:128
	v_mul_f32_e32 v48, v48, v66
	v_mul_f32_e32 v49, v49, v66
	v_mul_f32_e32 v50, v50, v66
	v_mul_f32_e32 v51, v51, v66
	v_mul_f32_e32 v56, v56, v66
	v_mul_f32_e32 v57, v57, v66
	v_mul_f32_e32 v58, v58, v66
	v_mul_f32_e32 v59, v59, v66
	v_cvt_pk_bf16_f32 v84, v48, v49
	v_cvt_pk_bf16_f32 v85, v50, v51
	v_cvt_pk_bf16_f32 v86, v56, v57
	v_cvt_pk_bf16_f32 v87, v58, v59
	s_nop 1
	v_permlane16_swap_b32_e32 v84, v86
	v_permlane16_swap_b32_e32 v85, v87
	s_nop 1
	global_store_dwordx4 v70, v[84:87], s[58:59] offset:192
	v_mul_f32_e32 v4, v4, v67
	v_mul_f32_e32 v5, v5, v67
	v_mul_f32_e32 v6, v6, v67
	v_mul_f32_e32 v7, v7, v67
	v_mul_f32_e32 v12, v12, v67
	v_mul_f32_e32 v13, v13, v67
	v_mul_f32_e32 v14, v14, v67
	v_mul_f32_e32 v15, v15, v67
	v_cvt_pk_bf16_f32 v88, v4, v5
	v_cvt_pk_bf16_f32 v89, v6, v7
	v_cvt_pk_bf16_f32 v90, v12, v13
	v_cvt_pk_bf16_f32 v91, v14, v15
	s_nop 1
	v_permlane16_swap_b32_e32 v88, v90
	v_permlane16_swap_b32_e32 v89, v91
	s_nop 1
	global_store_dwordx4 v71, v[88:91], s[58:59] offset:0
	v_mul_f32_e32 v20, v20, v67
	v_mul_f32_e32 v21, v21, v67
	v_mul_f32_e32 v22, v22, v67
	v_mul_f32_e32 v23, v23, v67
	v_mul_f32_e32 v28, v28, v67
	v_mul_f32_e32 v29, v29, v67
	v_mul_f32_e32 v30, v30, v67
	v_mul_f32_e32 v31, v31, v67
	v_cvt_pk_bf16_f32 v92, v20, v21
	v_cvt_pk_bf16_f32 v93, v22, v23
	v_cvt_pk_bf16_f32 v94, v28, v29
	v_cvt_pk_bf16_f32 v95, v30, v31
	s_nop 1
	v_permlane16_swap_b32_e32 v92, v94
	v_permlane16_swap_b32_e32 v93, v95
	s_nop 1
	global_store_dwordx4 v71, v[92:95], s[58:59] offset:64
	v_mul_f32_e32 v36, v36, v67
	v_mul_f32_e32 v37, v37, v67
	v_mul_f32_e32 v38, v38, v67
	v_mul_f32_e32 v39, v39, v67
	v_mul_f32_e32 v44, v44, v67
	v_mul_f32_e32 v45, v45, v67
	v_mul_f32_e32 v46, v46, v67
	v_mul_f32_e32 v47, v47, v67
	v_cvt_pk_bf16_f32 v72, v36, v37
	v_cvt_pk_bf16_f32 v73, v38, v39
	v_cvt_pk_bf16_f32 v74, v44, v45
	v_cvt_pk_bf16_f32 v75, v46, v47
	s_nop 1
	v_permlane16_swap_b32_e32 v72, v74
	v_permlane16_swap_b32_e32 v73, v75
	s_nop 1
	global_store_dwordx4 v71, v[72:75], s[58:59] offset:128
	v_mul_f32_e32 v52, v52, v67
	v_mul_f32_e32 v53, v53, v67
	v_mul_f32_e32 v54, v54, v67
	v_mul_f32_e32 v55, v55, v67
	v_mul_f32_e32 v60, v60, v67
	v_mul_f32_e32 v61, v61, v67
	v_mul_f32_e32 v62, v62, v67
	v_mul_f32_e32 v63, v63, v67
	v_cvt_pk_bf16_f32 v76, v52, v53
	v_cvt_pk_bf16_f32 v77, v54, v55
	v_cvt_pk_bf16_f32 v78, v60, v61
	v_cvt_pk_bf16_f32 v79, v62, v63
	s_nop 1
	v_permlane16_swap_b32_e32 v76, v78
	v_permlane16_swap_b32_e32 v77, v79
	s_nop 1
	global_store_dwordx4 v71, v[76:79], s[58:59] offset:192
	s_barrier
